# p8 GEMM K-loop (in-proj, gates): issue priority given to the LDS-read/stage part instead of the MFMA cluster (the read part is the critical one at the barrier hand-off)
# speedup vs baseline: 1.0142x; 1.0014x over previous
.LBB0_226:
	s_add_u32 s30, s26, 0xfffc0080
	s_addc_u32 s31, s27, -1
	s_and_b64 s[28:29], s[28:29], exec
	s_cselect_b32 s31, s21, s31
	s_cselect_b32 s30, s20, s30
	s_cselect_b32 s29, s23, s52
	s_cselect_b32 s28, s22, s49
	s_add_i32 s54, 0, 0x10000
	v_add_u32_e32 v2, s54, v163
	ds_read_b128 v[132:135], v2
	ds_read_b128 v[136:139], v2 offset:1024
	ds_read_b128 v[140:143], v2 offset:2048
	ds_read_b128 v[144:147], v2 offset:3072
	v_lshl_add_u64 v[160:161], s[26:27], 0, v[156:157]
	s_add_i32 m0, s36, 0xc000
	ds_read_b128 v[166:169], v164
	ds_read_b128 v[170:173], v164 offset:1024
	ds_read_b128 v[174:177], v164 offset:2048
	ds_read_b128 v[178:181], v164 offset:3072
	ds_read_b128 v[182:185], v164 offset:4096
	ds_read_b128 v[186:189], v164 offset:5120
	ds_read_b128 v[190:193], v164 offset:6144
	ds_read_b128 v[194:197], v164 offset:7168
	global_load_lds_dwordx4 v[160:161], off
	v_lshl_add_u64 v[160:161], s[26:27], 0, v[158:159]
	s_add_i32 m0, s36, 0xe000
	s_nop 0
	global_load_lds_dwordx4 v[160:161], off
	s_waitcnt lgkmcnt(8)
	s_barrier
	s_waitcnt lgkmcnt(0)
	s_setprio 0
	s_waitcnt lgkmcnt(0)
	v_mfma_f32_16x16x32_bf16 v[128:131], v[132:135], v[166:169], v[128:131]
	v_mfma_f32_16x16x32_bf16 v[124:127], v[140:143], v[166:169], v[124:127]
	v_mfma_f32_16x16x32_bf16 v[116:119], v[132:135], v[174:177], v[116:119]
	v_mfma_f32_16x16x32_bf16 v[108:111], v[140:143], v[174:177], v[108:111]
	v_mfma_f32_16x16x32_bf16 v[100:103], v[132:135], v[182:185], v[100:103]
	v_mfma_f32_16x16x32_bf16 v[92:95], v[140:143], v[182:185], v[92:95]
	v_mfma_f32_16x16x32_bf16 v[84:87], v[132:135], v[190:193], v[84:87]
	v_mfma_f32_16x16x32_bf16 v[76:79], v[140:143], v[190:193], v[76:79]
	v_mfma_f32_16x16x32_bf16 v[128:131], v[136:139], v[170:173], v[128:131]
	v_mfma_f32_16x16x32_bf16 v[124:127], v[144:147], v[170:173], v[124:127]
	v_mfma_f32_16x16x32_bf16 v[116:119], v[136:139], v[178:181], v[116:119]
	v_mfma_f32_16x16x32_bf16 v[108:111], v[144:147], v[178:181], v[108:111]
	v_mfma_f32_16x16x32_bf16 v[100:103], v[136:139], v[186:189], v[100:103]
	v_mfma_f32_16x16x32_bf16 v[92:95], v[144:147], v[186:189], v[92:95]
	v_mfma_f32_16x16x32_bf16 v[84:87], v[136:139], v[194:197], v[84:87]
	v_mfma_f32_16x16x32_bf16 v[76:79], v[144:147], v[194:197], v[76:79]
	s_setprio 1
	s_barrier
	s_add_i32 s56, 0, 0x14000
	s_add_i32 s54, s54, s35
	v_add_u32_e32 v2, s56, v163
	v_lshl_add_u64 v[160:161], s[28:29], 0, v[150:151]
	s_mov_b32 m0, s54
	ds_read_b128 v[198:201], v2
	ds_read_b128 v[202:205], v2 offset:1024
	ds_read_b128 v[206:209], v2 offset:2048
	ds_read_b128 v[210:213], v2 offset:3072
	global_load_lds_dwordx4 v[160:161], off
	v_lshl_add_u64 v[222:223], s[28:29], 0, v[154:155]
	s_add_i32 m0, s54, 0x2000
	s_nop 0
	global_load_lds_dwordx4 v[222:223], off
	s_barrier
	s_waitcnt lgkmcnt(0)
	s_setprio 0
	s_waitcnt lgkmcnt(0)
	v_mfma_f32_16x16x32_bf16 v[120:123], v[198:201], v[166:169], v[120:123]
	v_mfma_f32_16x16x32_bf16 v[112:115], v[206:209], v[166:169], v[112:115]
	v_mfma_f32_16x16x32_bf16 v[104:107], v[198:201], v[174:177], v[104:107]
	v_mfma_f32_16x16x32_bf16 v[96:99], v[206:209], v[174:177], v[96:99]
	v_mfma_f32_16x16x32_bf16 v[88:91], v[198:201], v[182:185], v[88:91]
	v_mfma_f32_16x16x32_bf16 v[80:83], v[206:209], v[182:185], v[80:83]
	v_mfma_f32_16x16x32_bf16 v[72:75], v[198:201], v[190:193], v[72:75]
	v_mfma_f32_16x16x32_bf16 v[68:71], v[206:209], v[190:193], v[68:71]
	v_mfma_f32_16x16x32_bf16 v[120:123], v[202:205], v[170:173], v[120:123]
	v_mfma_f32_16x16x32_bf16 v[112:115], v[210:213], v[170:173], v[112:115]
	v_mfma_f32_16x16x32_bf16 v[104:107], v[202:205], v[178:181], v[104:107]
	v_mfma_f32_16x16x32_bf16 v[96:99], v[210:213], v[178:181], v[96:99]
	v_mfma_f32_16x16x32_bf16 v[88:91], v[202:205], v[186:189], v[88:91]
	v_mfma_f32_16x16x32_bf16 v[80:83], v[210:213], v[186:189], v[80:83]
	v_mfma_f32_16x16x32_bf16 v[72:75], v[202:205], v[194:197], v[72:75]
	v_mfma_f32_16x16x32_bf16 v[68:71], v[210:213], v[194:197], v[68:71]
	s_setprio 1
	s_mov_b32 m0, s36
	v_lshl_add_u64 v[224:225], s[30:31], 0, v[148:149]
	s_barrier
	ds_read_b128 v[166:169], v164 offset:16384
	ds_read_b128 v[170:173], v164 offset:17408
	ds_read_b128 v[174:177], v164 offset:18432
	ds_read_b128 v[178:181], v164 offset:19456
	ds_read_b128 v[182:185], v164 offset:20480
	ds_read_b128 v[186:189], v164 offset:21504
	ds_read_b128 v[190:193], v164 offset:22528
	ds_read_b128 v[194:197], v164 offset:23552
	global_load_lds_dwordx4 v[224:225], off
	v_lshl_add_u64 v[230:231], s[30:31], 0, v[152:153]
	s_mov_b32 m0, s37
	s_nop 0
	global_load_lds_dwordx4 v[230:231], off
	s_barrier
	s_waitcnt lgkmcnt(0)
	s_setprio 0
	s_waitcnt lgkmcnt(0)
	v_mfma_f32_16x16x32_bf16 v[64:67], v[132:135], v[166:169], v[64:67]
	v_mfma_f32_16x16x32_bf16 v[60:63], v[140:143], v[166:169], v[60:63]
	v_mfma_f32_16x16x32_bf16 v[52:55], v[132:135], v[174:177], v[52:55]
	v_mfma_f32_16x16x32_bf16 v[44:47], v[140:143], v[174:177], v[44:47]
	v_mfma_f32_16x16x32_bf16 v[36:39], v[132:135], v[182:185], v[36:39]
	v_mfma_f32_16x16x32_bf16 v[28:31], v[140:143], v[182:185], v[28:31]
	v_mfma_f32_16x16x32_bf16 v[20:23], v[132:135], v[190:193], v[20:23]
	v_mfma_f32_16x16x32_bf16 v[12:15], v[140:143], v[190:193], v[12:15]
	v_mfma_f32_16x16x32_bf16 v[64:67], v[136:139], v[170:173], v[64:67]
	v_mfma_f32_16x16x32_bf16 v[60:63], v[144:147], v[170:173], v[60:63]
	v_mfma_f32_16x16x32_bf16 v[52:55], v[136:139], v[178:181], v[52:55]
	v_mfma_f32_16x16x32_bf16 v[44:47], v[144:147], v[178:181], v[44:47]
	v_mfma_f32_16x16x32_bf16 v[36:39], v[136:139], v[186:189], v[36:39]
	v_mfma_f32_16x16x32_bf16 v[28:31], v[144:147], v[186:189], v[28:31]
	v_mfma_f32_16x16x32_bf16 v[20:23], v[136:139], v[194:197], v[20:23]
	v_mfma_f32_16x16x32_bf16 v[12:15], v[144:147], v[194:197], v[12:15]
	s_setprio 1
	s_barrier
	s_add_u32 s54, s28, 0x40000
	s_addc_u32 s55, s29, 0
	s_add_i32 s56, s56, s35
	v_lshl_add_u64 v[132:133], s[54:55], 0, v[150:151]
	s_mov_b32 m0, s56
	s_nop 0
	global_load_lds_dwordx4 v[132:133], off
	v_lshl_add_u64 v[132:133], s[54:55], 0, v[154:155]
	s_add_i32 m0, s56, 0x2000
	s_nop 0
	global_load_lds_dwordx4 v[132:133], off
	s_waitcnt vmcnt(6)
	s_barrier
	s_setprio 0
	v_mfma_f32_16x16x32_bf16 v[56:59], v[198:201], v[166:169], v[56:59]
	v_mfma_f32_16x16x32_bf16 v[48:51], v[206:209], v[166:169], v[48:51]
	v_mfma_f32_16x16x32_bf16 v[40:43], v[198:201], v[174:177], v[40:43]
	v_mfma_f32_16x16x32_bf16 v[32:35], v[206:209], v[174:177], v[32:35]
	v_mfma_f32_16x16x32_bf16 v[24:27], v[198:201], v[182:185], v[24:27]
	v_mfma_f32_16x16x32_bf16 v[16:19], v[206:209], v[182:185], v[16:19]
	v_mfma_f32_16x16x32_bf16 v[8:11], v[198:201], v[190:193], v[8:11]
	v_mfma_f32_16x16x32_bf16 v[4:7], v[206:209], v[190:193], v[4:7]
	v_mfma_f32_16x16x32_bf16 v[56:59], v[202:205], v[170:173], v[56:59]
	v_mfma_f32_16x16x32_bf16 v[48:51], v[210:213], v[170:173], v[48:51]
	v_mfma_f32_16x16x32_bf16 v[40:43], v[202:205], v[178:181], v[40:43]
	v_mfma_f32_16x16x32_bf16 v[32:35], v[210:213], v[178:181], v[32:35]
	v_mfma_f32_16x16x32_bf16 v[24:27], v[202:205], v[186:189], v[24:27]
	v_mfma_f32_16x16x32_bf16 v[16:19], v[210:213], v[186:189], v[16:19]
	v_mfma_f32_16x16x32_bf16 v[8:11], v[202:205], v[194:197], v[8:11]
	v_mfma_f32_16x16x32_bf16 v[4:7], v[210:213], v[194:197], v[4:7]
	s_setprio 1
	s_add_i32 s54, 0, 0x18000
	v_add_u32_e32 v2, s54, v163
	s_barrier
	ds_read_b128 v[132:135], v2
	ds_read_b128 v[136:139], v2 offset:1024
	ds_read_b128 v[140:143], v2 offset:2048
	ds_read_b128 v[144:147], v2 offset:3072
	s_add_u32 s30, s30, 0x40000
	s_addc_u32 s31, s31, 0
	s_mov_b32 m0, s38
	v_lshl_add_u64 v[198:199], s[30:31], 0, v[148:149]
	ds_read_b128 v[166:169], v164 offset:32768
	ds_read_b128 v[170:173], v164 offset:33792
	ds_read_b128 v[174:177], v164 offset:34816
	ds_read_b128 v[178:181], v164 offset:35840
	ds_read_b128 v[182:185], v164 offset:36864
	ds_read_b128 v[186:189], v164 offset:37888
	ds_read_b128 v[190:193], v164 offset:38912
	ds_read_b128 v[194:197], v164 offset:39936
	global_load_lds_dwordx4 v[198:199], off
	v_lshl_add_u64 v[198:199], s[30:31], 0, v[152:153]
	s_mov_b32 m0, s39
	s_nop 0
	global_load_lds_dwordx4 v[198:199], off
	s_waitcnt lgkmcnt(8)
	s_barrier
	s_waitcnt lgkmcnt(0)
	s_setprio 0
	s_waitcnt lgkmcnt(0)
	v_mfma_f32_16x16x32_bf16 v[128:131], v[132:135], v[166:169], v[128:131]
	v_mfma_f32_16x16x32_bf16 v[124:127], v[140:143], v[166:169], v[124:127]
	v_mfma_f32_16x16x32_bf16 v[116:119], v[132:135], v[174:177], v[116:119]
	v_mfma_f32_16x16x32_bf16 v[108:111], v[140:143], v[174:177], v[108:111]
	v_mfma_f32_16x16x32_bf16 v[100:103], v[132:135], v[182:185], v[100:103]
	v_mfma_f32_16x16x32_bf16 v[92:95], v[140:143], v[182:185], v[92:95]
	v_mfma_f32_16x16x32_bf16 v[84:87], v[132:135], v[190:193], v[84:87]
	v_mfma_f32_16x16x32_bf16 v[76:79], v[140:143], v[190:193], v[76:79]
	v_mfma_f32_16x16x32_bf16 v[128:131], v[136:139], v[170:173], v[128:131]
	v_mfma_f32_16x16x32_bf16 v[124:127], v[144:147], v[170:173], v[124:127]
	v_mfma_f32_16x16x32_bf16 v[116:119], v[136:139], v[178:181], v[116:119]
	v_mfma_f32_16x16x32_bf16 v[108:111], v[144:147], v[178:181], v[108:111]
	v_mfma_f32_16x16x32_bf16 v[100:103], v[136:139], v[186:189], v[100:103]
	v_mfma_f32_16x16x32_bf16 v[92:95], v[144:147], v[186:189], v[92:95]
	v_mfma_f32_16x16x32_bf16 v[84:87], v[136:139], v[194:197], v[84:87]
	v_mfma_f32_16x16x32_bf16 v[76:79], v[144:147], v[194:197], v[76:79]
	s_setprio 1
	s_barrier
	s_add_i32 s30, 0, 0x1c000
	s_add_i32 s31, s54, s35
	v_add_u32_e32 v2, s30, v163
	v_lshl_add_u64 v[160:161], v[160:161], 0, s[60:61]
	s_mov_b32 m0, s31
	ds_read_b128 v[198:201], v2
	ds_read_b128 v[202:205], v2 offset:1024
	ds_read_b128 v[206:209], v2 offset:2048
	ds_read_b128 v[210:213], v2 offset:3072
	global_load_lds_dwordx4 v[160:161], off
	v_lshl_add_u64 v[160:161], v[222:223], 0, s[60:61]
	s_add_i32 m0, s31, 0x2000
	s_nop 0
	global_load_lds_dwordx4 v[160:161], off
	s_barrier
	s_waitcnt lgkmcnt(0)
	s_setprio 0
	s_waitcnt lgkmcnt(0)
	v_mfma_f32_16x16x32_bf16 v[120:123], v[198:201], v[166:169], v[120:123]
	v_mfma_f32_16x16x32_bf16 v[112:115], v[206:209], v[166:169], v[112:115]
	v_mfma_f32_16x16x32_bf16 v[104:107], v[198:201], v[174:177], v[104:107]
	v_mfma_f32_16x16x32_bf16 v[96:99], v[206:209], v[174:177], v[96:99]
	v_mfma_f32_16x16x32_bf16 v[88:91], v[198:201], v[182:185], v[88:91]
	v_mfma_f32_16x16x32_bf16 v[80:83], v[206:209], v[182:185], v[80:83]
	v_mfma_f32_16x16x32_bf16 v[72:75], v[198:201], v[190:193], v[72:75]
	v_mfma_f32_16x16x32_bf16 v[68:71], v[206:209], v[190:193], v[68:71]
	v_mfma_f32_16x16x32_bf16 v[120:123], v[202:205], v[170:173], v[120:123]
	v_mfma_f32_16x16x32_bf16 v[112:115], v[210:213], v[170:173], v[112:115]
	v_mfma_f32_16x16x32_bf16 v[104:107], v[202:205], v[178:181], v[104:107]
	v_mfma_f32_16x16x32_bf16 v[96:99], v[210:213], v[178:181], v[96:99]
	v_mfma_f32_16x16x32_bf16 v[88:91], v[202:205], v[186:189], v[88:91]
	v_mfma_f32_16x16x32_bf16 v[80:83], v[210:213], v[186:189], v[80:83]
	v_mfma_f32_16x16x32_bf16 v[72:75], v[202:205], v[194:197], v[72:75]
	v_mfma_f32_16x16x32_bf16 v[68:71], v[210:213], v[194:197], v[68:71]
	s_setprio 1
	s_mov_b32 m0, s42
	v_lshl_add_u64 v[160:161], v[224:225], 0, s[60:61]
	s_barrier
	ds_read_b128 v[166:169], v164 offset:49152
	ds_read_b128 v[170:173], v164 offset:50176
	ds_read_b128 v[174:177], v164 offset:51200
	ds_read_b128 v[178:181], v164 offset:52224
	ds_read_b128 v[182:185], v164 offset:53248
	ds_read_b128 v[186:189], v164 offset:54272
	ds_read_b128 v[190:193], v164 offset:55296
	ds_read_b128 v[194:197], v164 offset:56320
	global_load_lds_dwordx4 v[160:161], off
	v_lshl_add_u64 v[160:161], v[230:231], 0, s[60:61]
	s_mov_b32 m0, s43
	s_nop 0
	global_load_lds_dwordx4 v[160:161], off
	s_barrier
	s_waitcnt lgkmcnt(0)
	s_setprio 0
	s_waitcnt lgkmcnt(0)
	v_mfma_f32_16x16x32_bf16 v[64:67], v[132:135], v[166:169], v[64:67]
	v_mfma_f32_16x16x32_bf16 v[60:63], v[140:143], v[166:169], v[60:63]
	v_mfma_f32_16x16x32_bf16 v[52:55], v[132:135], v[174:177], v[52:55]
	v_mfma_f32_16x16x32_bf16 v[44:47], v[140:143], v[174:177], v[44:47]
	v_mfma_f32_16x16x32_bf16 v[36:39], v[132:135], v[182:185], v[36:39]
	v_mfma_f32_16x16x32_bf16 v[28:31], v[140:143], v[182:185], v[28:31]
	v_mfma_f32_16x16x32_bf16 v[20:23], v[132:135], v[190:193], v[20:23]
	v_mfma_f32_16x16x32_bf16 v[12:15], v[140:143], v[190:193], v[12:15]
	v_mfma_f32_16x16x32_bf16 v[64:67], v[136:139], v[170:173], v[64:67]
	v_mfma_f32_16x16x32_bf16 v[60:63], v[144:147], v[170:173], v[60:63]
	v_mfma_f32_16x16x32_bf16 v[52:55], v[136:139], v[178:181], v[52:55]
	v_mfma_f32_16x16x32_bf16 v[44:47], v[144:147], v[178:181], v[44:47]
	v_mfma_f32_16x16x32_bf16 v[36:39], v[136:139], v[186:189], v[36:39]
	v_mfma_f32_16x16x32_bf16 v[28:31], v[144:147], v[186:189], v[28:31]
	v_mfma_f32_16x16x32_bf16 v[20:23], v[136:139], v[194:197], v[20:23]
	v_mfma_f32_16x16x32_bf16 v[12:15], v[144:147], v[194:197], v[12:15]
	s_setprio 1
	s_barrier
	s_add_u32 s28, s28, 0x40080
	s_addc_u32 s29, s29, 0
	s_add_i32 s30, s30, s35
	v_lshl_add_u64 v[132:133], s[28:29], 0, v[150:151]
	s_mov_b32 m0, s30
	s_nop 0
	global_load_lds_dwordx4 v[132:133], off
	v_lshl_add_u64 v[132:133], s[28:29], 0, v[154:155]
	s_add_i32 m0, s30, 0x2000
	s_nop 0
	global_load_lds_dwordx4 v[132:133], off
	s_waitcnt vmcnt(6)
	s_barrier
	s_setprio 0
	v_mfma_f32_16x16x32_bf16 v[56:59], v[198:201], v[166:169], v[56:59]
	v_mfma_f32_16x16x32_bf16 v[48:51], v[206:209], v[166:169], v[48:51]
	v_mfma_f32_16x16x32_bf16 v[40:43], v[198:201], v[174:177], v[40:43]
	v_mfma_f32_16x16x32_bf16 v[32:35], v[206:209], v[174:177], v[32:35]
	v_mfma_f32_16x16x32_bf16 v[24:27], v[198:201], v[182:185], v[24:27]
	v_mfma_f32_16x16x32_bf16 v[16:19], v[206:209], v[182:185], v[16:19]
	v_mfma_f32_16x16x32_bf16 v[8:11], v[198:201], v[190:193], v[8:11]
	v_mfma_f32_16x16x32_bf16 v[4:7], v[206:209], v[190:193], v[4:7]
	v_mfma_f32_16x16x32_bf16 v[56:59], v[202:205], v[170:173], v[56:59]
	v_mfma_f32_16x16x32_bf16 v[48:51], v[210:213], v[170:173], v[48:51]
	v_mfma_f32_16x16x32_bf16 v[40:43], v[202:205], v[178:181], v[40:43]
	v_mfma_f32_16x16x32_bf16 v[32:35], v[210:213], v[178:181], v[32:35]
	v_mfma_f32_16x16x32_bf16 v[24:27], v[202:205], v[186:189], v[24:27]
	v_mfma_f32_16x16x32_bf16 v[16:19], v[210:213], v[186:189], v[16:19]
	v_mfma_f32_16x16x32_bf16 v[8:11], v[202:205], v[194:197], v[8:11]
	v_mfma_f32_16x16x32_bf16 v[4:7], v[210:213], v[194:197], v[4:7]
	s_setprio 1
	s_add_i32 s53, s53, 2
	s_add_u32 s26, s26, 0x100
	s_addc_u32 s27, s27, 0
	s_add_u32 s49, s49, 0x100
	s_addc_u32 s52, s52, 0
	s_cmp_gt_u32 s53, 13
	s_barrier
	s_cbranch_scc1 .LBB0_230

.LBB0_230:
	s_setprio 0
	s_lshl_b32 s15, s48, 10
	s_and_b32 s15, s15, 0x400
	s_add_i32 s15, s15, 0
	v_mov_b32_e32 v135, v162
	s_add_i32 s15, s15, 0x20000
	s_lshl_b32 s17, s46, 8
	s_lshl_b32 s24, s47, 8
	s_add_i32 s25, s47, -12
	s_cmp_lt_u32 s25, 3
	v_and_b32_e32 v160, 15, v135
	v_bfe_u32 v134, v135, 4, 2
	s_mov_b64 s[26:27], -1
	s_cbranch_scc1 .LBB0_232
	v_or_b32_e32 v2, s40, v160
	v_lshl_add_u32 v161, v2, 2, s15
	ds_read2_b32 v[140:141], v161 offset1:16
	v_add_u32_e32 v165, s17, v2
	v_mov_b64_e32 v[132:133], s[12:13]
	s_ashr_i32 s25, s24, 31
	v_mad_i64_i32 v[136:137], s[26:27], v165, s33, v[132:133]
	s_lshl_b64 s[26:27], s[24:25], 1
	s_nop 0
	v_lshl_add_u64 v[136:137], v[136:137], 0, s[26:27]
	v_lshl_add_u64 v[136:137], v[136:137], 0, s[50:51]
	v_lshlrev_b32_e32 v2, 4, v134
	v_lshl_add_u64 v[142:143], v[136:137], 0, v[2:3]
	s_waitcnt lgkmcnt(0)
	v_pk_mul_f32 v[138:139], v[130:131], v[140:141] op_sel_hi:[1,0]
	v_pk_mul_f32 v[136:137], v[128:129], v[140:141] op_sel_hi:[1,0]
	v_pk_mul_f32 v[144:145], v[126:127], v[140:141] op_sel_hi:[1,0]
	v_pk_mul_f32 v[146:147], v[124:125], v[140:141] op_sel_hi:[1,0]
	v_cvt_pk_bf16_f32 v136, v136, v137
	v_cvt_pk_bf16_f32 v137, v138, v139
	v_cvt_pk_bf16_f32 v138, v146, v147
	v_cvt_pk_bf16_f32 v139, v144, v145
	global_store_dwordx4 v[142:143], v[136:139], off
	v_pk_mul_f32 v[144:145], v[114:115], v[140:141] op_sel_hi:[1,0]
	v_pk_mul_f32 v[146:147], v[112:113], v[140:141] op_sel_hi:[1,0]
	v_pk_mul_f32 v[138:139], v[122:123], v[140:141] op_sel_hi:[1,0]
	v_pk_mul_f32 v[136:137], v[120:121], v[140:141] op_sel_hi:[1,0]
	v_mov_b32_e32 v140, v141
	v_cvt_pk_bf16_f32 v136, v136, v137
	v_cvt_pk_bf16_f32 v137, v138, v139
	v_cvt_pk_bf16_f32 v138, v146, v147
	v_cvt_pk_bf16_f32 v139, v144, v145
	global_store_dwordx4 v[142:143], v[136:139], off offset:256
	v_pk_mul_f32 v[144:145], v[110:111], v[140:141] op_sel_hi:[1,0]
	v_pk_mul_f32 v[146:147], v[108:109], v[140:141] op_sel_hi:[1,0]
	v_add_u32_e32 v136, 16, v165
	v_mad_i64_i32 v[136:137], s[28:29], v136, s33, v[132:133]
	v_lshl_add_u64 v[136:137], v[136:137], 0, s[26:27]
	v_lshl_add_u64 v[136:137], v[136:137], 0, s[50:51]
	v_lshl_add_u64 v[142:143], v[136:137], 0, v[2:3]
	v_pk_mul_f32 v[138:139], v[118:119], v[140:141] op_sel_hi:[1,0]
	v_pk_mul_f32 v[136:137], v[116:117], v[140:141] op_sel_hi:[1,0]
	s_nop 0
	v_cvt_pk_bf16_f32 v136, v136, v137
	v_cvt_pk_bf16_f32 v137, v138, v139
	v_cvt_pk_bf16_f32 v138, v146, v147
	v_cvt_pk_bf16_f32 v139, v144, v145
	global_store_dwordx4 v[142:143], v[136:139], off
	v_pk_mul_f32 v[144:145], v[98:99], v[140:141] op_sel_hi:[1,0]
	s_nop 0
	v_pk_mul_f32 v[138:139], v[106:107], v[140:141] op_sel_hi:[1,0]
	v_pk_mul_f32 v[136:137], v[104:105], v[140:141] op_sel_hi:[1,0]
	v_pk_mul_f32 v[140:141], v[96:97], v[140:141] op_sel_hi:[1,0]
	v_cvt_pk_bf16_f32 v136, v136, v137
	v_cvt_pk_bf16_f32 v137, v138, v139
	v_cvt_pk_bf16_f32 v138, v140, v141
	v_cvt_pk_bf16_f32 v139, v144, v145
	ds_read2_b32 v[140:141], v161 offset0:32 offset1:48
	global_store_dwordx4 v[142:143], v[136:139], off offset:256
	s_waitcnt lgkmcnt(0)
	v_pk_mul_f32 v[144:145], v[94:95], v[140:141] op_sel_hi:[1,0]
	v_add_u32_e32 v136, 32, v165
	v_mad_i64_i32 v[136:137], s[28:29], v136, s33, v[132:133]
	v_lshl_add_u64 v[136:137], v[136:137], 0, s[26:27]
	v_lshl_add_u64 v[136:137], v[136:137], 0, s[50:51]
	v_lshl_add_u64 v[142:143], v[136:137], 0, v[2:3]
	v_pk_mul_f32 v[138:139], v[102:103], v[140:141] op_sel_hi:[1,0]
	v_pk_mul_f32 v[136:137], v[100:101], v[140:141] op_sel_hi:[1,0]
	v_pk_mul_f32 v[146:147], v[92:93], v[140:141] op_sel_hi:[1,0]
	v_cvt_pk_bf16_f32 v136, v136, v137
	v_cvt_pk_bf16_f32 v137, v138, v139
	v_cvt_pk_bf16_f32 v138, v146, v147
	v_cvt_pk_bf16_f32 v139, v144, v145
	global_store_dwordx4 v[142:143], v[136:139], off
	v_pk_mul_f32 v[144:145], v[82:83], v[140:141] op_sel_hi:[1,0]
	v_pk_mul_f32 v[146:147], v[80:81], v[140:141] op_sel_hi:[1,0]
	v_pk_mul_f32 v[138:139], v[90:91], v[140:141] op_sel_hi:[1,0]
	v_pk_mul_f32 v[136:137], v[88:89], v[140:141] op_sel_hi:[1,0]
	v_mov_b32_e32 v140, v141
	v_cvt_pk_bf16_f32 v136, v136, v137
	v_cvt_pk_bf16_f32 v137, v138, v139
	v_cvt_pk_bf16_f32 v138, v146, v147
	v_cvt_pk_bf16_f32 v139, v144, v145
	global_store_dwordx4 v[142:143], v[136:139], off offset:256
	v_pk_mul_f32 v[144:145], v[78:79], v[140:141] op_sel_hi:[1,0]
	v_pk_mul_f32 v[146:147], v[76:77], v[140:141] op_sel_hi:[1,0]
	v_add_u32_e32 v136, 48, v165
	v_mad_i64_i32 v[136:137], s[28:29], v136, s33, v[132:133]
	v_lshl_add_u64 v[136:137], v[136:137], 0, s[26:27]
	v_lshl_add_u64 v[136:137], v[136:137], 0, s[50:51]
	v_lshl_add_u64 v[142:143], v[136:137], 0, v[2:3]
	v_pk_mul_f32 v[138:139], v[86:87], v[140:141] op_sel_hi:[1,0]
	v_pk_mul_f32 v[136:137], v[84:85], v[140:141] op_sel_hi:[1,0]
	s_nop 0
	v_cvt_pk_bf16_f32 v136, v136, v137
	v_cvt_pk_bf16_f32 v137, v138, v139
	v_cvt_pk_bf16_f32 v138, v146, v147
	v_cvt_pk_bf16_f32 v139, v144, v145
	global_store_dwordx4 v[142:143], v[136:139], off
	v_pk_mul_f32 v[144:145], v[70:71], v[140:141] op_sel_hi:[1,0]
	s_nop 0
	v_pk_mul_f32 v[138:139], v[74:75], v[140:141] op_sel_hi:[1,0]
	v_pk_mul_f32 v[136:137], v[72:73], v[140:141] op_sel_hi:[1,0]
	v_pk_mul_f32 v[140:141], v[68:69], v[140:141] op_sel_hi:[1,0]
	v_cvt_pk_bf16_f32 v136, v136, v137
	v_cvt_pk_bf16_f32 v137, v138, v139
	v_cvt_pk_bf16_f32 v138, v140, v141
	v_cvt_pk_bf16_f32 v139, v144, v145
	ds_read2_b32 v[140:141], v161 offset0:128 offset1:144
	global_store_dwordx4 v[142:143], v[136:139], off offset:256
	s_waitcnt lgkmcnt(0)
	v_pk_mul_f32 v[144:145], v[62:63], v[140:141] op_sel_hi:[1,0]
	v_add_u32_e32 v136, 0x80, v165
	v_mad_i64_i32 v[136:137], s[28:29], v136, s33, v[132:133]
	v_lshl_add_u64 v[136:137], v[136:137], 0, s[26:27]
	v_lshl_add_u64 v[136:137], v[136:137], 0, s[50:51]
	v_lshl_add_u64 v[142:143], v[136:137], 0, v[2:3]
	v_pk_mul_f32 v[138:139], v[66:67], v[140:141] op_sel_hi:[1,0]
	v_pk_mul_f32 v[136:137], v[64:65], v[140:141] op_sel_hi:[1,0]
	v_pk_mul_f32 v[146:147], v[60:61], v[140:141] op_sel_hi:[1,0]
	v_cvt_pk_bf16_f32 v136, v136, v137
	v_cvt_pk_bf16_f32 v137, v138, v139
	v_cvt_pk_bf16_f32 v138, v146, v147
	v_cvt_pk_bf16_f32 v139, v144, v145
	global_store_dwordx4 v[142:143], v[136:139], off
	v_pk_mul_f32 v[144:145], v[50:51], v[140:141] op_sel_hi:[1,0]
	v_pk_mul_f32 v[146:147], v[48:49], v[140:141] op_sel_hi:[1,0]
	v_pk_mul_f32 v[138:139], v[58:59], v[140:141] op_sel_hi:[1,0]
	v_pk_mul_f32 v[136:137], v[56:57], v[140:141] op_sel_hi:[1,0]
	v_mov_b32_e32 v140, v141
	v_cvt_pk_bf16_f32 v136, v136, v137
	v_cvt_pk_bf16_f32 v137, v138, v139
	v_cvt_pk_bf16_f32 v138, v146, v147
	v_cvt_pk_bf16_f32 v139, v144, v145
	global_store_dwordx4 v[142:143], v[136:139], off offset:256
	v_pk_mul_f32 v[144:145], v[46:47], v[140:141] op_sel_hi:[1,0]
	v_pk_mul_f32 v[146:147], v[44:45], v[140:141] op_sel_hi:[1,0]
	v_add_u32_e32 v136, 0x90, v165
	v_mad_i64_i32 v[136:137], s[28:29], v136, s33, v[132:133]
	v_lshl_add_u64 v[136:137], v[136:137], 0, s[26:27]
	v_lshl_add_u64 v[136:137], v[136:137], 0, s[50:51]
	v_lshl_add_u64 v[142:143], v[136:137], 0, v[2:3]
	v_pk_mul_f32 v[138:139], v[54:55], v[140:141] op_sel_hi:[1,0]
	v_pk_mul_f32 v[136:137], v[52:53], v[140:141] op_sel_hi:[1,0]
	s_nop 0
	v_cvt_pk_bf16_f32 v136, v136, v137
	v_cvt_pk_bf16_f32 v137, v138, v139
	v_cvt_pk_bf16_f32 v138, v146, v147
	v_cvt_pk_bf16_f32 v139, v144, v145
	global_store_dwordx4 v[142:143], v[136:139], off
	v_pk_mul_f32 v[144:145], v[34:35], v[140:141] op_sel_hi:[1,0]
	s_nop 0
	v_pk_mul_f32 v[138:139], v[42:43], v[140:141] op_sel_hi:[1,0]
	v_pk_mul_f32 v[136:137], v[40:41], v[140:141] op_sel_hi:[1,0]
	v_pk_mul_f32 v[140:141], v[32:33], v[140:141] op_sel_hi:[1,0]
	v_cvt_pk_bf16_f32 v136, v136, v137
	v_cvt_pk_bf16_f32 v137, v138, v139
	v_cvt_pk_bf16_f32 v138, v140, v141
	v_cvt_pk_bf16_f32 v139, v144, v145
	ds_read2_b32 v[140:141], v161 offset0:160 offset1:176
	global_store_dwordx4 v[142:143], v[136:139], off offset:256
	s_waitcnt lgkmcnt(0)
	v_pk_mul_f32 v[144:145], v[30:31], v[140:141] op_sel_hi:[1,0]
	v_add_u32_e32 v136, 0xa0, v165
	v_mad_i64_i32 v[136:137], s[28:29], v136, s33, v[132:133]
	v_lshl_add_u64 v[136:137], v[136:137], 0, s[26:27]
	v_lshl_add_u64 v[136:137], v[136:137], 0, s[50:51]
	v_lshl_add_u64 v[142:143], v[136:137], 0, v[2:3]
	v_pk_mul_f32 v[138:139], v[38:39], v[140:141] op_sel_hi:[1,0]
	v_pk_mul_f32 v[136:137], v[36:37], v[140:141] op_sel_hi:[1,0]
	v_pk_mul_f32 v[146:147], v[28:29], v[140:141] op_sel_hi:[1,0]
	v_cvt_pk_bf16_f32 v136, v136, v137
	v_cvt_pk_bf16_f32 v137, v138, v139
	v_cvt_pk_bf16_f32 v138, v146, v147
	v_cvt_pk_bf16_f32 v139, v144, v145
	global_store_dwordx4 v[142:143], v[136:139], off
	v_pk_mul_f32 v[144:145], v[18:19], v[140:141] op_sel_hi:[1,0]
	v_pk_mul_f32 v[146:147], v[16:17], v[140:141] op_sel_hi:[1,0]
	v_pk_mul_f32 v[138:139], v[26:27], v[140:141] op_sel_hi:[1,0]
	v_pk_mul_f32 v[136:137], v[24:25], v[140:141] op_sel_hi:[1,0]
	s_nop 0
	v_cvt_pk_bf16_f32 v136, v136, v137
	v_cvt_pk_bf16_f32 v137, v138, v139
	v_cvt_pk_bf16_f32 v138, v146, v147
	v_cvt_pk_bf16_f32 v139, v144, v145
	global_store_dwordx4 v[142:143], v[136:139], off offset:256
	s_nop 1
	v_add_u32_e32 v136, 0xb0, v165
	v_mad_i64_i32 v[132:133], s[28:29], v136, s33, v[132:133]
	v_lshl_add_u64 v[132:133], v[132:133], 0, s[26:27]
	v_lshl_add_u64 v[132:133], v[132:133], 0, s[50:51]
	v_lshl_add_u64 v[132:133], v[132:133], 0, v[2:3]
	v_mov_b32_e32 v2, v141
	v_pk_mul_f32 v[138:139], v[22:23], v[2:3] op_sel_hi:[1,0]
	v_pk_mul_f32 v[136:137], v[20:21], v[2:3] op_sel_hi:[1,0]
	v_pk_mul_f32 v[140:141], v[14:15], v[2:3] op_sel_hi:[1,0]
	v_pk_mul_f32 v[142:143], v[12:13], v[2:3] op_sel_hi:[1,0]
	v_cvt_pk_bf16_f32 v136, v136, v137
	v_cvt_pk_bf16_f32 v137, v138, v139
	v_cvt_pk_bf16_f32 v138, v142, v143
	v_cvt_pk_bf16_f32 v139, v140, v141
	global_store_dwordx4 v[132:133], v[136:139], off
	v_pk_mul_f32 v[140:141], v[6:7], v[2:3] op_sel_hi:[1,0]
	v_pk_mul_f32 v[142:143], v[4:5], v[2:3] op_sel_hi:[1,0]
	v_pk_mul_f32 v[138:139], v[10:11], v[2:3] op_sel_hi:[1,0]
	v_pk_mul_f32 v[136:137], v[8:9], v[2:3] op_sel_hi:[1,0]
	s_mov_b64 s[26:27], 0
	v_cvt_pk_bf16_f32 v136, v136, v137
	v_cvt_pk_bf16_f32 v137, v138, v139
	v_cvt_pk_bf16_f32 v138, v142, v143
	v_cvt_pk_bf16_f32 v139, v140, v141
	global_store_dwordx4 v[132:133], v[136:139], off offset:256

.Lmy_bias_skip:
	s_add_u32 s38, s34, 0xfffc0080
	s_addc_u32 s39, s35, -1
	s_and_b64 s[36:37], s[36:37], exec
	s_cselect_b32 s39, s27, s39
	s_cselect_b32 s38, s26, s38
	s_cselect_b32 s37, s29, s63
	s_cselect_b32 s36, s28, s62
	s_add_i32 s65, 0, 0x10000
	v_add_u32_e32 v2, s65, v163
	ds_read_b128 v[132:135], v2
	ds_read_b128 v[136:139], v2 offset:1024
	ds_read_b128 v[140:143], v2 offset:2048
	ds_read_b128 v[144:147], v2 offset:3072
	v_lshl_add_u64 v[160:161], s[34:35], 0, v[156:157]
	s_add_i32 m0, s42, 0xc000
	ds_read_b128 v[166:169], v164
	ds_read_b128 v[170:173], v164 offset:1024
	ds_read_b128 v[174:177], v164 offset:2048
	ds_read_b128 v[178:181], v164 offset:3072
	ds_read_b128 v[182:185], v164 offset:4096
	ds_read_b128 v[186:189], v164 offset:5120
	ds_read_b128 v[190:193], v164 offset:6144
	ds_read_b128 v[194:197], v164 offset:7168
	global_load_lds_dwordx4 v[160:161], off
	v_lshl_add_u64 v[160:161], s[34:35], 0, v[158:159]
	s_add_i32 m0, s42, 0xe000
	s_nop 0
	global_load_lds_dwordx4 v[160:161], off
	s_waitcnt lgkmcnt(8)
	s_barrier
	s_waitcnt lgkmcnt(0)
	s_setprio 0
	s_waitcnt lgkmcnt(0)
	v_mfma_f32_16x16x32_bf16 v[128:131], v[132:135], v[166:169], v[128:131]
	v_mfma_f32_16x16x32_bf16 v[124:127], v[140:143], v[166:169], v[124:127]
	v_mfma_f32_16x16x32_bf16 v[112:115], v[132:135], v[174:177], v[112:115]
	v_mfma_f32_16x16x32_bf16 v[108:111], v[140:143], v[174:177], v[108:111]
	v_mfma_f32_16x16x32_bf16 v[96:99], v[132:135], v[182:185], v[96:99]
	v_mfma_f32_16x16x32_bf16 v[92:95], v[140:143], v[182:185], v[92:95]
	v_mfma_f32_16x16x32_bf16 v[80:83], v[132:135], v[190:193], v[80:83]
	v_mfma_f32_16x16x32_bf16 v[76:79], v[140:143], v[190:193], v[76:79]
	v_mfma_f32_16x16x32_bf16 v[128:131], v[136:139], v[170:173], v[128:131]
	v_mfma_f32_16x16x32_bf16 v[124:127], v[144:147], v[170:173], v[124:127]
	v_mfma_f32_16x16x32_bf16 v[112:115], v[136:139], v[178:181], v[112:115]
	v_mfma_f32_16x16x32_bf16 v[108:111], v[144:147], v[178:181], v[108:111]
	v_mfma_f32_16x16x32_bf16 v[96:99], v[136:139], v[186:189], v[96:99]
	v_mfma_f32_16x16x32_bf16 v[92:95], v[144:147], v[186:189], v[92:95]
	v_mfma_f32_16x16x32_bf16 v[80:83], v[136:139], v[194:197], v[80:83]
	v_mfma_f32_16x16x32_bf16 v[76:79], v[144:147], v[194:197], v[76:79]
	s_setprio 1
	s_barrier
	s_add_i32 s68, 0, 0x14000
	s_add_i32 s65, s65, s41
	v_add_u32_e32 v2, s68, v163
	v_lshl_add_u64 v[160:161], s[36:37], 0, v[150:151]
	s_mov_b32 m0, s65
	ds_read_b128 v[198:201], v2
	ds_read_b128 v[202:205], v2 offset:1024
	ds_read_b128 v[206:209], v2 offset:2048
	ds_read_b128 v[210:213], v2 offset:3072
	global_load_lds_dwordx4 v[160:161], off
	v_lshl_add_u64 v[222:223], s[36:37], 0, v[154:155]
	s_add_i32 m0, s65, 0x2000
	s_nop 0
	global_load_lds_dwordx4 v[222:223], off
	s_barrier
	s_waitcnt lgkmcnt(0)
	s_setprio 0
	s_waitcnt lgkmcnt(0)
	v_mfma_f32_16x16x32_bf16 v[120:123], v[198:201], v[166:169], v[120:123]
	v_mfma_f32_16x16x32_bf16 v[116:119], v[206:209], v[166:169], v[116:119]
	v_mfma_f32_16x16x32_bf16 v[104:107], v[198:201], v[174:177], v[104:107]
	v_mfma_f32_16x16x32_bf16 v[100:103], v[206:209], v[174:177], v[100:103]
	v_mfma_f32_16x16x32_bf16 v[88:91], v[198:201], v[182:185], v[88:91]
	v_mfma_f32_16x16x32_bf16 v[84:87], v[206:209], v[182:185], v[84:87]
	v_mfma_f32_16x16x32_bf16 v[72:75], v[198:201], v[190:193], v[72:75]
	v_mfma_f32_16x16x32_bf16 v[68:71], v[206:209], v[190:193], v[68:71]
	v_mfma_f32_16x16x32_bf16 v[120:123], v[202:205], v[170:173], v[120:123]
	v_mfma_f32_16x16x32_bf16 v[116:119], v[210:213], v[170:173], v[116:119]
	v_mfma_f32_16x16x32_bf16 v[104:107], v[202:205], v[178:181], v[104:107]
	v_mfma_f32_16x16x32_bf16 v[100:103], v[210:213], v[178:181], v[100:103]
	v_mfma_f32_16x16x32_bf16 v[88:91], v[202:205], v[186:189], v[88:91]
	v_mfma_f32_16x16x32_bf16 v[84:87], v[210:213], v[186:189], v[84:87]
	v_mfma_f32_16x16x32_bf16 v[72:75], v[202:205], v[194:197], v[72:75]
	v_mfma_f32_16x16x32_bf16 v[68:71], v[210:213], v[194:197], v[68:71]
	s_setprio 1
	s_mov_b32 m0, s42
	v_lshl_add_u64 v[224:225], s[38:39], 0, v[148:149]
	s_barrier
	ds_read_b128 v[166:169], v164 offset:16384
	ds_read_b128 v[170:173], v164 offset:17408
	ds_read_b128 v[174:177], v164 offset:18432
	ds_read_b128 v[178:181], v164 offset:19456
	ds_read_b128 v[182:185], v164 offset:20480
	ds_read_b128 v[186:189], v164 offset:21504
	ds_read_b128 v[190:193], v164 offset:22528
	ds_read_b128 v[194:197], v164 offset:23552
	global_load_lds_dwordx4 v[224:225], off
	v_lshl_add_u64 v[230:231], s[38:39], 0, v[152:153]
	s_mov_b32 m0, s43
	s_nop 0
	global_load_lds_dwordx4 v[230:231], off
	s_barrier
	s_waitcnt lgkmcnt(0)
	s_setprio 0
	s_waitcnt lgkmcnt(0)
	v_mfma_f32_16x16x32_bf16 v[64:67], v[132:135], v[166:169], v[64:67]
	v_mfma_f32_16x16x32_bf16 v[60:63], v[140:143], v[166:169], v[60:63]
	v_mfma_f32_16x16x32_bf16 v[48:51], v[132:135], v[174:177], v[48:51]
	v_mfma_f32_16x16x32_bf16 v[44:47], v[140:143], v[174:177], v[44:47]
	v_mfma_f32_16x16x32_bf16 v[32:35], v[132:135], v[182:185], v[32:35]
	v_mfma_f32_16x16x32_bf16 v[28:31], v[140:143], v[182:185], v[28:31]
	v_mfma_f32_16x16x32_bf16 v[16:19], v[132:135], v[190:193], v[16:19]
	v_mfma_f32_16x16x32_bf16 v[12:15], v[140:143], v[190:193], v[12:15]
	v_mfma_f32_16x16x32_bf16 v[64:67], v[136:139], v[170:173], v[64:67]
	v_mfma_f32_16x16x32_bf16 v[60:63], v[144:147], v[170:173], v[60:63]
	v_mfma_f32_16x16x32_bf16 v[48:51], v[136:139], v[178:181], v[48:51]
	v_mfma_f32_16x16x32_bf16 v[44:47], v[144:147], v[178:181], v[44:47]
	v_mfma_f32_16x16x32_bf16 v[32:35], v[136:139], v[186:189], v[32:35]
	v_mfma_f32_16x16x32_bf16 v[28:31], v[144:147], v[186:189], v[28:31]
	v_mfma_f32_16x16x32_bf16 v[16:19], v[136:139], v[194:197], v[16:19]
	v_mfma_f32_16x16x32_bf16 v[12:15], v[144:147], v[194:197], v[12:15]
	s_setprio 1
	s_barrier
	s_add_u32 s66, s36, 0x40000
	s_addc_u32 s67, s37, 0
	s_add_i32 s65, s68, s41
	v_lshl_add_u64 v[132:133], s[66:67], 0, v[150:151]
	s_mov_b32 m0, s65
	s_nop 0
	global_load_lds_dwordx4 v[132:133], off
	v_lshl_add_u64 v[132:133], s[66:67], 0, v[154:155]
	s_add_i32 m0, s65, 0x2000
	s_nop 0
	global_load_lds_dwordx4 v[132:133], off
	s_waitcnt vmcnt(6)
	s_barrier
	s_setprio 0
	v_mfma_f32_16x16x32_bf16 v[56:59], v[198:201], v[166:169], v[56:59]
	v_mfma_f32_16x16x32_bf16 v[52:55], v[206:209], v[166:169], v[52:55]
	v_mfma_f32_16x16x32_bf16 v[40:43], v[198:201], v[174:177], v[40:43]
	v_mfma_f32_16x16x32_bf16 v[36:39], v[206:209], v[174:177], v[36:39]
	v_mfma_f32_16x16x32_bf16 v[24:27], v[198:201], v[182:185], v[24:27]
	v_mfma_f32_16x16x32_bf16 v[20:23], v[206:209], v[182:185], v[20:23]
	v_mfma_f32_16x16x32_bf16 v[8:11], v[198:201], v[190:193], v[8:11]
	v_mfma_f32_16x16x32_bf16 v[4:7], v[206:209], v[190:193], v[4:7]
	v_mfma_f32_16x16x32_bf16 v[56:59], v[202:205], v[170:173], v[56:59]
	v_mfma_f32_16x16x32_bf16 v[52:55], v[210:213], v[170:173], v[52:55]
	v_mfma_f32_16x16x32_bf16 v[40:43], v[202:205], v[178:181], v[40:43]
	v_mfma_f32_16x16x32_bf16 v[36:39], v[210:213], v[178:181], v[36:39]
	v_mfma_f32_16x16x32_bf16 v[24:27], v[202:205], v[186:189], v[24:27]
	v_mfma_f32_16x16x32_bf16 v[20:23], v[210:213], v[186:189], v[20:23]
	v_mfma_f32_16x16x32_bf16 v[8:11], v[202:205], v[194:197], v[8:11]
	v_mfma_f32_16x16x32_bf16 v[4:7], v[210:213], v[194:197], v[4:7]
	s_setprio 1
	s_add_i32 s65, 0, 0x18000
	v_add_u32_e32 v2, s65, v163
	s_barrier
	ds_read_b128 v[132:135], v2
	ds_read_b128 v[136:139], v2 offset:1024
	ds_read_b128 v[140:143], v2 offset:2048
	ds_read_b128 v[144:147], v2 offset:3072
	s_add_u32 s38, s38, 0x40000
	s_addc_u32 s39, s39, 0
	s_mov_b32 m0, s44
	v_lshl_add_u64 v[198:199], s[38:39], 0, v[148:149]
	ds_read_b128 v[166:169], v164 offset:32768
	ds_read_b128 v[170:173], v164 offset:33792
	ds_read_b128 v[174:177], v164 offset:34816
	ds_read_b128 v[178:181], v164 offset:35840
	ds_read_b128 v[182:185], v164 offset:36864
	ds_read_b128 v[186:189], v164 offset:37888
	ds_read_b128 v[190:193], v164 offset:38912
	ds_read_b128 v[194:197], v164 offset:39936
	global_load_lds_dwordx4 v[198:199], off
	v_lshl_add_u64 v[198:199], s[38:39], 0, v[152:153]
	s_mov_b32 m0, s45
	s_nop 0
	global_load_lds_dwordx4 v[198:199], off
	s_waitcnt lgkmcnt(8)
	s_barrier
	s_waitcnt lgkmcnt(0)
	s_setprio 0
	s_waitcnt lgkmcnt(0)
	v_mfma_f32_16x16x32_bf16 v[128:131], v[132:135], v[166:169], v[128:131]
	v_mfma_f32_16x16x32_bf16 v[124:127], v[140:143], v[166:169], v[124:127]
	v_mfma_f32_16x16x32_bf16 v[112:115], v[132:135], v[174:177], v[112:115]
	v_mfma_f32_16x16x32_bf16 v[108:111], v[140:143], v[174:177], v[108:111]
	v_mfma_f32_16x16x32_bf16 v[96:99], v[132:135], v[182:185], v[96:99]
	v_mfma_f32_16x16x32_bf16 v[92:95], v[140:143], v[182:185], v[92:95]
	v_mfma_f32_16x16x32_bf16 v[80:83], v[132:135], v[190:193], v[80:83]
	v_mfma_f32_16x16x32_bf16 v[76:79], v[140:143], v[190:193], v[76:79]
	v_mfma_f32_16x16x32_bf16 v[128:131], v[136:139], v[170:173], v[128:131]
	v_mfma_f32_16x16x32_bf16 v[124:127], v[144:147], v[170:173], v[124:127]
	v_mfma_f32_16x16x32_bf16 v[112:115], v[136:139], v[178:181], v[112:115]
	v_mfma_f32_16x16x32_bf16 v[108:111], v[144:147], v[178:181], v[108:111]
	v_mfma_f32_16x16x32_bf16 v[96:99], v[136:139], v[186:189], v[96:99]
	v_mfma_f32_16x16x32_bf16 v[92:95], v[144:147], v[186:189], v[92:95]
	v_mfma_f32_16x16x32_bf16 v[80:83], v[136:139], v[194:197], v[80:83]
	v_mfma_f32_16x16x32_bf16 v[76:79], v[144:147], v[194:197], v[76:79]
	s_setprio 1
	s_barrier
	s_add_i32 s38, 0, 0x1c000
	s_add_i32 s39, s65, s41
	v_add_u32_e32 v2, s38, v163
	v_lshl_add_u64 v[160:161], v[160:161], 0, s[60:61]
	s_mov_b32 m0, s39
	ds_read_b128 v[198:201], v2
	ds_read_b128 v[202:205], v2 offset:1024
	ds_read_b128 v[206:209], v2 offset:2048
	ds_read_b128 v[210:213], v2 offset:3072
	global_load_lds_dwordx4 v[160:161], off
	v_lshl_add_u64 v[160:161], v[222:223], 0, s[60:61]
	s_add_i32 m0, s39, 0x2000
	s_nop 0
	global_load_lds_dwordx4 v[160:161], off
	s_barrier
	s_waitcnt lgkmcnt(0)
	s_setprio 0
	s_waitcnt lgkmcnt(0)
	v_mfma_f32_16x16x32_bf16 v[120:123], v[198:201], v[166:169], v[120:123]
	v_mfma_f32_16x16x32_bf16 v[116:119], v[206:209], v[166:169], v[116:119]
	v_mfma_f32_16x16x32_bf16 v[104:107], v[198:201], v[174:177], v[104:107]
	v_mfma_f32_16x16x32_bf16 v[100:103], v[206:209], v[174:177], v[100:103]
	v_mfma_f32_16x16x32_bf16 v[88:91], v[198:201], v[182:185], v[88:91]
	v_mfma_f32_16x16x32_bf16 v[84:87], v[206:209], v[182:185], v[84:87]
	v_mfma_f32_16x16x32_bf16 v[72:75], v[198:201], v[190:193], v[72:75]
	v_mfma_f32_16x16x32_bf16 v[68:71], v[206:209], v[190:193], v[68:71]
	v_mfma_f32_16x16x32_bf16 v[120:123], v[202:205], v[170:173], v[120:123]
	v_mfma_f32_16x16x32_bf16 v[116:119], v[210:213], v[170:173], v[116:119]
	v_mfma_f32_16x16x32_bf16 v[104:107], v[202:205], v[178:181], v[104:107]
	v_mfma_f32_16x16x32_bf16 v[100:103], v[210:213], v[178:181], v[100:103]
	v_mfma_f32_16x16x32_bf16 v[88:91], v[202:205], v[186:189], v[88:91]
	v_mfma_f32_16x16x32_bf16 v[84:87], v[210:213], v[186:189], v[84:87]
	v_mfma_f32_16x16x32_bf16 v[72:75], v[202:205], v[194:197], v[72:75]
	v_mfma_f32_16x16x32_bf16 v[68:71], v[210:213], v[194:197], v[68:71]
	s_setprio 1
	s_mov_b32 m0, s48
	v_lshl_add_u64 v[160:161], v[224:225], 0, s[60:61]
	s_barrier
	ds_read_b128 v[166:169], v164 offset:49152
	ds_read_b128 v[170:173], v164 offset:50176
	ds_read_b128 v[174:177], v164 offset:51200
	ds_read_b128 v[178:181], v164 offset:52224
	ds_read_b128 v[182:185], v164 offset:53248
	ds_read_b128 v[186:189], v164 offset:54272
	ds_read_b128 v[190:193], v164 offset:55296
	ds_read_b128 v[194:197], v164 offset:56320
	global_load_lds_dwordx4 v[160:161], off
	v_lshl_add_u64 v[160:161], v[230:231], 0, s[60:61]
	s_mov_b32 m0, s49
	s_nop 0
	global_load_lds_dwordx4 v[160:161], off
	s_barrier
	s_waitcnt lgkmcnt(0)
	s_setprio 0
	s_waitcnt lgkmcnt(0)
	v_mfma_f32_16x16x32_bf16 v[64:67], v[132:135], v[166:169], v[64:67]
	v_mfma_f32_16x16x32_bf16 v[60:63], v[140:143], v[166:169], v[60:63]
	v_mfma_f32_16x16x32_bf16 v[48:51], v[132:135], v[174:177], v[48:51]
	v_mfma_f32_16x16x32_bf16 v[44:47], v[140:143], v[174:177], v[44:47]
	v_mfma_f32_16x16x32_bf16 v[32:35], v[132:135], v[182:185], v[32:35]
	v_mfma_f32_16x16x32_bf16 v[28:31], v[140:143], v[182:185], v[28:31]
	v_mfma_f32_16x16x32_bf16 v[16:19], v[132:135], v[190:193], v[16:19]
	v_mfma_f32_16x16x32_bf16 v[12:15], v[140:143], v[190:193], v[12:15]
	v_mfma_f32_16x16x32_bf16 v[64:67], v[136:139], v[170:173], v[64:67]
	v_mfma_f32_16x16x32_bf16 v[60:63], v[144:147], v[170:173], v[60:63]
	v_mfma_f32_16x16x32_bf16 v[48:51], v[136:139], v[178:181], v[48:51]
	v_mfma_f32_16x16x32_bf16 v[44:47], v[144:147], v[178:181], v[44:47]
	v_mfma_f32_16x16x32_bf16 v[32:35], v[136:139], v[186:189], v[32:35]
	v_mfma_f32_16x16x32_bf16 v[28:31], v[144:147], v[186:189], v[28:31]
	v_mfma_f32_16x16x32_bf16 v[16:19], v[136:139], v[194:197], v[16:19]
	v_mfma_f32_16x16x32_bf16 v[12:15], v[144:147], v[194:197], v[12:15]
	s_setprio 1
	s_barrier
	s_add_u32 s36, s36, 0x40080
	s_addc_u32 s37, s37, 0
	s_add_i32 s38, s38, s41
	v_lshl_add_u64 v[132:133], s[36:37], 0, v[150:151]
	s_mov_b32 m0, s38
	s_nop 0
	global_load_lds_dwordx4 v[132:133], off
	v_lshl_add_u64 v[132:133], s[36:37], 0, v[154:155]
	s_add_i32 m0, s38, 0x2000
	s_nop 0
	global_load_lds_dwordx4 v[132:133], off
	s_waitcnt vmcnt(6)
	s_barrier
	s_setprio 0
	v_mfma_f32_16x16x32_bf16 v[56:59], v[198:201], v[166:169], v[56:59]
	v_mfma_f32_16x16x32_bf16 v[52:55], v[206:209], v[166:169], v[52:55]
	v_mfma_f32_16x16x32_bf16 v[40:43], v[198:201], v[174:177], v[40:43]
	v_mfma_f32_16x16x32_bf16 v[36:39], v[206:209], v[174:177], v[36:39]
	v_mfma_f32_16x16x32_bf16 v[24:27], v[198:201], v[182:185], v[24:27]
	v_mfma_f32_16x16x32_bf16 v[20:23], v[206:209], v[182:185], v[20:23]
	v_mfma_f32_16x16x32_bf16 v[8:11], v[198:201], v[190:193], v[8:11]
	v_mfma_f32_16x16x32_bf16 v[4:7], v[206:209], v[190:193], v[4:7]
	v_mfma_f32_16x16x32_bf16 v[56:59], v[202:205], v[170:173], v[56:59]
	v_mfma_f32_16x16x32_bf16 v[52:55], v[210:213], v[170:173], v[52:55]
	v_mfma_f32_16x16x32_bf16 v[40:43], v[202:205], v[178:181], v[40:43]
	v_mfma_f32_16x16x32_bf16 v[36:39], v[210:213], v[178:181], v[36:39]
	v_mfma_f32_16x16x32_bf16 v[24:27], v[202:205], v[186:189], v[24:27]
	v_mfma_f32_16x16x32_bf16 v[20:23], v[210:213], v[186:189], v[20:23]
	v_mfma_f32_16x16x32_bf16 v[8:11], v[202:205], v[194:197], v[8:11]
	v_mfma_f32_16x16x32_bf16 v[4:7], v[210:213], v[194:197], v[4:7]
	s_setprio 1
	s_add_i32 s64, s64, 2
	s_add_u32 s34, s34, 0x100
	s_addc_u32 s35, s35, 0
	s_add_u32 s62, s62, 0x100
	s_addc_u32 s63, s63, 0
	s_cmp_gt_u32 s64, 13
	s_barrier
	s_cbranch_scc1 .LBB0_1981

.LBB0_1981:
	s_setprio 0
	s_lshl_b32 s21, s50, 10
	s_and_b32 s21, s21, 0x400
	s_add_i32 s21, s21, 0
	v_mov_b32_e32 v134, v162
	s_add_i32 s21, s21, 0x20000
	s_lshl_b32 s30, s19, 8
	s_cmp_lt_i32 s19, 18
	v_and_b32_e32 v165, 15, v134
	v_bfe_u32 v166, v134, 4, 2
	s_mov_b64 s[34:35], -1
	s_cbranch_scc0 .LBB0_1987
	s_lshl_b32 s36, s58, 8
	s_add_i32 s19, s19, -12
	s_cmp_lt_u32 s19, 3
	s_cbranch_scc1 .LBB0_1984
	v_or_b32_e32 v2, s46, v165
	v_lshl_add_u32 v135, v2, 2, s21
	ds_read2_b32 v[140:141], v135 offset1:16
	v_add_u32_e32 v160, s36, v2
	v_mov_b64_e32 v[132:133], s[16:17]
	s_ashr_i32 s31, s30, 31
	v_mad_i64_i32 v[136:137], s[34:35], v160, s33, v[132:133]
	s_lshl_b64 s[34:35], s[30:31], 1
	s_nop 0
	v_lshl_add_u64 v[136:137], v[136:137], 0, s[34:35]
	s_mov_b32 s19, s51
	v_lshl_add_u64 v[136:137], v[136:137], 0, s[18:19]
	v_lshlrev_b32_e32 v2, 4, v166
	v_lshl_add_u64 v[142:143], v[136:137], 0, v[2:3]
	s_waitcnt lgkmcnt(0)
	v_pk_mul_f32 v[138:139], v[130:131], v[140:141] op_sel_hi:[1,0]
	v_pk_mul_f32 v[136:137], v[128:129], v[140:141] op_sel_hi:[1,0]
	v_pk_mul_f32 v[144:145], v[126:127], v[140:141] op_sel_hi:[1,0]
	v_pk_mul_f32 v[146:147], v[124:125], v[140:141] op_sel_hi:[1,0]
	v_cvt_pk_bf16_f32 v136, v136, v137
	v_cvt_pk_bf16_f32 v137, v138, v139
	v_cvt_pk_bf16_f32 v138, v146, v147
	v_cvt_pk_bf16_f32 v139, v144, v145
	global_store_dwordx4 v[142:143], v[136:139], off
	v_pk_mul_f32 v[144:145], v[118:119], v[140:141] op_sel_hi:[1,0]
	v_pk_mul_f32 v[146:147], v[116:117], v[140:141] op_sel_hi:[1,0]
	v_pk_mul_f32 v[138:139], v[122:123], v[140:141] op_sel_hi:[1,0]
	v_pk_mul_f32 v[136:137], v[120:121], v[140:141] op_sel_hi:[1,0]
	v_mov_b32_e32 v140, v141
	v_cvt_pk_bf16_f32 v136, v136, v137
	v_cvt_pk_bf16_f32 v137, v138, v139
	v_cvt_pk_bf16_f32 v138, v146, v147
	v_cvt_pk_bf16_f32 v139, v144, v145
	global_store_dwordx4 v[142:143], v[136:139], off offset:256
	v_pk_mul_f32 v[144:145], v[110:111], v[140:141] op_sel_hi:[1,0]
	v_pk_mul_f32 v[146:147], v[108:109], v[140:141] op_sel_hi:[1,0]
	v_add_u32_e32 v136, 16, v160
	v_mad_i64_i32 v[136:137], s[38:39], v136, s33, v[132:133]
	v_lshl_add_u64 v[136:137], v[136:137], 0, s[34:35]
	v_lshl_add_u64 v[136:137], v[136:137], 0, s[18:19]
	v_lshl_add_u64 v[142:143], v[136:137], 0, v[2:3]
	v_pk_mul_f32 v[138:139], v[114:115], v[140:141] op_sel_hi:[1,0]
	v_pk_mul_f32 v[136:137], v[112:113], v[140:141] op_sel_hi:[1,0]
	s_nop 0
	v_cvt_pk_bf16_f32 v136, v136, v137
	v_cvt_pk_bf16_f32 v137, v138, v139
	v_cvt_pk_bf16_f32 v138, v146, v147
	v_cvt_pk_bf16_f32 v139, v144, v145
	global_store_dwordx4 v[142:143], v[136:139], off
	v_pk_mul_f32 v[144:145], v[102:103], v[140:141] op_sel_hi:[1,0]
	s_nop 0
	v_pk_mul_f32 v[138:139], v[106:107], v[140:141] op_sel_hi:[1,0]
	v_pk_mul_f32 v[136:137], v[104:105], v[140:141] op_sel_hi:[1,0]
	v_pk_mul_f32 v[140:141], v[100:101], v[140:141] op_sel_hi:[1,0]
	v_cvt_pk_bf16_f32 v136, v136, v137
	v_cvt_pk_bf16_f32 v137, v138, v139
	v_cvt_pk_bf16_f32 v138, v140, v141
	v_cvt_pk_bf16_f32 v139, v144, v145
	ds_read2_b32 v[140:141], v135 offset0:32 offset1:48
	global_store_dwordx4 v[142:143], v[136:139], off offset:256
	s_waitcnt lgkmcnt(0)
	v_pk_mul_f32 v[144:145], v[94:95], v[140:141] op_sel_hi:[1,0]
	v_add_u32_e32 v136, 32, v160
	v_mad_i64_i32 v[136:137], s[38:39], v136, s33, v[132:133]
	v_lshl_add_u64 v[136:137], v[136:137], 0, s[34:35]
	v_lshl_add_u64 v[136:137], v[136:137], 0, s[18:19]
	v_lshl_add_u64 v[142:143], v[136:137], 0, v[2:3]
	v_pk_mul_f32 v[138:139], v[98:99], v[140:141] op_sel_hi:[1,0]
	v_pk_mul_f32 v[136:137], v[96:97], v[140:141] op_sel_hi:[1,0]
	v_pk_mul_f32 v[146:147], v[92:93], v[140:141] op_sel_hi:[1,0]
	v_cvt_pk_bf16_f32 v136, v136, v137
	v_cvt_pk_bf16_f32 v137, v138, v139
	v_cvt_pk_bf16_f32 v138, v146, v147
	v_cvt_pk_bf16_f32 v139, v144, v145
	global_store_dwordx4 v[142:143], v[136:139], off
	v_pk_mul_f32 v[144:145], v[86:87], v[140:141] op_sel_hi:[1,0]
	v_pk_mul_f32 v[146:147], v[84:85], v[140:141] op_sel_hi:[1,0]
	v_pk_mul_f32 v[138:139], v[90:91], v[140:141] op_sel_hi:[1,0]
	v_pk_mul_f32 v[136:137], v[88:89], v[140:141] op_sel_hi:[1,0]
	v_mov_b32_e32 v140, v141
	v_cvt_pk_bf16_f32 v136, v136, v137
	v_cvt_pk_bf16_f32 v137, v138, v139
	v_cvt_pk_bf16_f32 v138, v146, v147
	v_cvt_pk_bf16_f32 v139, v144, v145
	global_store_dwordx4 v[142:143], v[136:139], off offset:256
	v_pk_mul_f32 v[144:145], v[78:79], v[140:141] op_sel_hi:[1,0]
	v_pk_mul_f32 v[146:147], v[76:77], v[140:141] op_sel_hi:[1,0]
	v_add_u32_e32 v136, 48, v160
	v_mad_i64_i32 v[136:137], s[38:39], v136, s33, v[132:133]
	v_lshl_add_u64 v[136:137], v[136:137], 0, s[34:35]
	v_lshl_add_u64 v[136:137], v[136:137], 0, s[18:19]
	v_lshl_add_u64 v[142:143], v[136:137], 0, v[2:3]
	v_pk_mul_f32 v[138:139], v[82:83], v[140:141] op_sel_hi:[1,0]
	v_pk_mul_f32 v[136:137], v[80:81], v[140:141] op_sel_hi:[1,0]
	s_nop 0
	v_cvt_pk_bf16_f32 v136, v136, v137
	v_cvt_pk_bf16_f32 v137, v138, v139
	v_cvt_pk_bf16_f32 v138, v146, v147
	v_cvt_pk_bf16_f32 v139, v144, v145
	global_store_dwordx4 v[142:143], v[136:139], off
	v_pk_mul_f32 v[144:145], v[70:71], v[140:141] op_sel_hi:[1,0]
	s_nop 0
	v_pk_mul_f32 v[138:139], v[74:75], v[140:141] op_sel_hi:[1,0]
	v_pk_mul_f32 v[136:137], v[72:73], v[140:141] op_sel_hi:[1,0]
	v_pk_mul_f32 v[140:141], v[68:69], v[140:141] op_sel_hi:[1,0]
	v_cvt_pk_bf16_f32 v136, v136, v137
	v_cvt_pk_bf16_f32 v137, v138, v139
	v_cvt_pk_bf16_f32 v138, v140, v141
	v_cvt_pk_bf16_f32 v139, v144, v145
	ds_read2_b32 v[140:141], v135 offset0:128 offset1:144
	global_store_dwordx4 v[142:143], v[136:139], off offset:256
	s_waitcnt lgkmcnt(0)
	v_pk_mul_f32 v[144:145], v[62:63], v[140:141] op_sel_hi:[1,0]
	v_add_u32_e32 v136, 0x80, v160
	v_mad_i64_i32 v[136:137], s[38:39], v136, s33, v[132:133]
	v_lshl_add_u64 v[136:137], v[136:137], 0, s[34:35]
	v_lshl_add_u64 v[136:137], v[136:137], 0, s[18:19]
	v_lshl_add_u64 v[142:143], v[136:137], 0, v[2:3]
	v_pk_mul_f32 v[138:139], v[66:67], v[140:141] op_sel_hi:[1,0]
	v_pk_mul_f32 v[136:137], v[64:65], v[140:141] op_sel_hi:[1,0]
	v_pk_mul_f32 v[146:147], v[60:61], v[140:141] op_sel_hi:[1,0]
	v_cvt_pk_bf16_f32 v136, v136, v137
	v_cvt_pk_bf16_f32 v137, v138, v139
	v_cvt_pk_bf16_f32 v138, v146, v147
	v_cvt_pk_bf16_f32 v139, v144, v145
	global_store_dwordx4 v[142:143], v[136:139], off
	v_pk_mul_f32 v[144:145], v[54:55], v[140:141] op_sel_hi:[1,0]
	v_pk_mul_f32 v[146:147], v[52:53], v[140:141] op_sel_hi:[1,0]
	v_pk_mul_f32 v[138:139], v[58:59], v[140:141] op_sel_hi:[1,0]
	v_pk_mul_f32 v[136:137], v[56:57], v[140:141] op_sel_hi:[1,0]
	v_mov_b32_e32 v140, v141
	v_cvt_pk_bf16_f32 v136, v136, v137
	v_cvt_pk_bf16_f32 v137, v138, v139
	v_cvt_pk_bf16_f32 v138, v146, v147
	v_cvt_pk_bf16_f32 v139, v144, v145
	global_store_dwordx4 v[142:143], v[136:139], off offset:256
	v_pk_mul_f32 v[144:145], v[46:47], v[140:141] op_sel_hi:[1,0]
	v_pk_mul_f32 v[146:147], v[44:45], v[140:141] op_sel_hi:[1,0]
	v_add_u32_e32 v136, 0x90, v160
	v_mad_i64_i32 v[136:137], s[38:39], v136, s33, v[132:133]
	v_lshl_add_u64 v[136:137], v[136:137], 0, s[34:35]
	v_lshl_add_u64 v[136:137], v[136:137], 0, s[18:19]
	v_lshl_add_u64 v[142:143], v[136:137], 0, v[2:3]
	v_pk_mul_f32 v[138:139], v[50:51], v[140:141] op_sel_hi:[1,0]
	v_pk_mul_f32 v[136:137], v[48:49], v[140:141] op_sel_hi:[1,0]
	s_nop 0
	v_cvt_pk_bf16_f32 v136, v136, v137
	v_cvt_pk_bf16_f32 v137, v138, v139
	v_cvt_pk_bf16_f32 v138, v146, v147
	v_cvt_pk_bf16_f32 v139, v144, v145
	global_store_dwordx4 v[142:143], v[136:139], off
	v_pk_mul_f32 v[144:145], v[38:39], v[140:141] op_sel_hi:[1,0]
	s_nop 0
	v_pk_mul_f32 v[138:139], v[42:43], v[140:141] op_sel_hi:[1,0]
	v_pk_mul_f32 v[136:137], v[40:41], v[140:141] op_sel_hi:[1,0]
	v_pk_mul_f32 v[140:141], v[36:37], v[140:141] op_sel_hi:[1,0]
	v_cvt_pk_bf16_f32 v136, v136, v137
	v_cvt_pk_bf16_f32 v137, v138, v139
	v_cvt_pk_bf16_f32 v138, v140, v141
	ds_read2_b32 v[140:141], v135 offset0:160 offset1:176
	v_cvt_pk_bf16_f32 v139, v144, v145
	v_add_u32_e32 v135, 0xa0, v160
	global_store_dwordx4 v[142:143], v[136:139], off offset:256
	s_waitcnt lgkmcnt(0)
	v_pk_mul_f32 v[144:145], v[30:31], v[140:141] op_sel_hi:[1,0]
	v_mad_i64_i32 v[136:137], s[38:39], v135, s33, v[132:133]
	v_lshl_add_u64 v[136:137], v[136:137], 0, s[34:35]
	v_lshl_add_u64 v[136:137], v[136:137], 0, s[18:19]
	v_add_u32_e32 v135, 0xb0, v160
	v_lshl_add_u64 v[142:143], v[136:137], 0, v[2:3]
	v_pk_mul_f32 v[138:139], v[34:35], v[140:141] op_sel_hi:[1,0]
	v_pk_mul_f32 v[136:137], v[32:33], v[140:141] op_sel_hi:[1,0]
	v_pk_mul_f32 v[146:147], v[28:29], v[140:141] op_sel_hi:[1,0]
	v_mad_i64_i32 v[132:133], s[38:39], v135, s33, v[132:133]
	v_cvt_pk_bf16_f32 v136, v136, v137
	v_cvt_pk_bf16_f32 v137, v138, v139
	v_cvt_pk_bf16_f32 v138, v146, v147
	v_cvt_pk_bf16_f32 v139, v144, v145
	v_lshl_add_u64 v[132:133], v[132:133], 0, s[34:35]
	global_store_dwordx4 v[142:143], v[136:139], off
	v_pk_mul_f32 v[144:145], v[22:23], v[140:141] op_sel_hi:[1,0]
	v_pk_mul_f32 v[146:147], v[20:21], v[140:141] op_sel_hi:[1,0]
	v_pk_mul_f32 v[138:139], v[26:27], v[140:141] op_sel_hi:[1,0]
	v_pk_mul_f32 v[136:137], v[24:25], v[140:141] op_sel_hi:[1,0]
	v_lshl_add_u64 v[132:133], v[132:133], 0, s[18:19]
	v_cvt_pk_bf16_f32 v136, v136, v137
	v_cvt_pk_bf16_f32 v137, v138, v139
	v_cvt_pk_bf16_f32 v138, v146, v147
	v_cvt_pk_bf16_f32 v139, v144, v145
	v_lshl_add_u64 v[132:133], v[132:133], 0, v[2:3]
	v_mov_b32_e32 v2, v141
	global_store_dwordx4 v[142:143], v[136:139], off offset:256
	v_pk_mul_f32 v[140:141], v[14:15], v[2:3] op_sel_hi:[1,0]
	v_pk_mul_f32 v[142:143], v[12:13], v[2:3] op_sel_hi:[1,0]
	v_pk_mul_f32 v[138:139], v[18:19], v[2:3] op_sel_hi:[1,0]
	v_pk_mul_f32 v[136:137], v[16:17], v[2:3] op_sel_hi:[1,0]
	s_mov_b64 s[34:35], 0
	v_cvt_pk_bf16_f32 v136, v136, v137
	v_cvt_pk_bf16_f32 v137, v138, v139
	v_cvt_pk_bf16_f32 v138, v142, v143
	v_cvt_pk_bf16_f32 v139, v140, v141
	global_store_dwordx4 v[132:133], v[136:139], off
	v_pk_mul_f32 v[140:141], v[6:7], v[2:3] op_sel_hi:[1,0]
	v_pk_mul_f32 v[142:143], v[4:5], v[2:3] op_sel_hi:[1,0]
	v_pk_mul_f32 v[138:139], v[10:11], v[2:3] op_sel_hi:[1,0]
	v_pk_mul_f32 v[136:137], v[8:9], v[2:3] op_sel_hi:[1,0]
	s_nop 0
	v_cvt_pk_bf16_f32 v136, v136, v137
	v_cvt_pk_bf16_f32 v137, v138, v139
	v_cvt_pk_bf16_f32 v138, v142, v143
	v_cvt_pk_bf16_f32 v139, v140, v141
	global_store_dwordx4 v[132:133], v[136:139], off offset:256
